# speedup vs baseline: 1.0572x; 1.0018x over previous
_Z11attn_kernelPKfS0_S0_PKcS2_PKDv4_jS0_S0_S0_S0_Pf:
	s_load_dwordx8 s[4:11], s[0:1], 0x0
	s_load_dwordx8 s[12:19], s[0:1], 0x20
	v_readfirstlane_b32 s20, v0
	s_bfe_u32 s28, s2, 0x10002
	s_lshr_b32 s29, s20, 6
	s_lshr_b32 s3, s20, 8
	s_bfe_u32 s30, s20, 0x20006
	s_lshr_b32 s31, s2, 3
	s_lshl_b32 s24, s28, 18
	s_waitcnt lgkmcnt(0)
	s_add_u32 s20, s10, s24
	s_addc_u32 s10, s11, 0
	s_and_b32 s21, s10, 0xffff
	s_add_u32 s24, s12, s24
	s_addc_u32 s10, s13, 0
	v_and_b32_e32 v1, 63, v0
	s_and_b32 s25, s10, 0xffff
	s_lshl_b32 s10, s30, 10
	s_lshl_b32 s38, s3, 12
	v_lshlrev_b32_e32 v2, 4, v1
	s_or_b32 s35, s10, s38
	v_lshl_or_b32 v2, s3, 17, v2
	s_cmp_lg_u32 0, -1
	v_or_b32_e32 v174, s10, v2
	s_cselect_b32 s10, 0, 0
	s_mov_b32 s36, 0
	s_mov_b32 s23, 0x20000
	s_mov_b32 s22, 0x40000
	s_add_i32 s33, s35, s10
	s_mov_b32 m0, s33
	s_nop 0
	buffer_load_dwordx4 v174, s[20:23], s36 offen lds
	s_mov_b32 s26, s22
	s_mov_b32 s27, s23
	s_add_i32 s34, s33, 0xc000
	s_mov_b32 m0, s34
	s_nop 0
	buffer_load_dwordx4 v174, s[24:27], s36 offen lds
	s_add_i32 s10, s33, 0x4000
	s_movk_i32 s37, 0x1000
	s_mov_b32 m0, s10
	s_nop 0
	buffer_load_dwordx4 v174, s[20:23], s37 offen lds
	s_add_i32 s10, s33, 0x8000
	s_movk_i32 s11, 0x2000
	s_mov_b32 m0, s10
	s_nop 0
	buffer_load_dwordx4 v174, s[20:23], s11 offen lds
	s_lshl_b32 s10, s2, 7
	s_and_b32 s10, s10, 0x380
	s_lshl_b32 s11, s31, 2
	s_add_i32 s10, s10, s11
	s_or_b32 s10, s30, s10
	v_and_b32_e32 v172, 31, v0
	v_lshl_or_b32 v140, s10, 7, v1
	v_mov_b32_e32 v141, 0
	v_lshl_add_u64 v[6:7], v[140:141], 4, s[14:15]
	v_ashrrev_i32_e32 v9, 31, v140
	v_mov_b32_e32 v8, v140
	v_lshl_or_b32 v140, s10, 5, v172
	v_lshlrev_b64 v[4:5], 2, v[140:141]
	v_lshl_add_u64 v[2:3], s[16:17], 0, v[4:5]
	global_load_dword v2, v[2:3], off
	v_lshl_add_u64 v[8:9], v[8:9], 4, s[14:15]
	global_load_dwordx4 v[116:119], v[6:7], off
	global_load_dwordx4 v[120:123], v[8:9], off offset:1024
	s_load_dwordx4 s[12:15], s[0:1], 0x40
	s_load_dwordx2 s[10:11], s[0:1], 0x50
	v_lshlrev_b32_e32 v173, 2, v1
	v_lshl_or_b32 v3, s28, 11, v173
	s_waitcnt lgkmcnt(0)
	global_load_dword v44, v3, s[14:15] offset:256
	global_load_dword v45, v3, s[14:15]
	v_bfe_u32 v175, v0, 5, 1
	v_lshlrev_b32_e32 v0, 11, v175
	v_lshlrev_b32_e32 v3, 4, v172
	s_add_i32 s0, s38, 0
	v_lshl_add_u64 v[4:5], s[12:13], 0, v[4:5]
	v_add3_u32 v176, s0, v0, v3
	global_load_dword v0, v[4:5], off
	v_lshrrev_b32_e32 v124, 2, v1
	v_lshrrev_b32_e32 v125, 4, v1
	v_xor_b32_e32 v124, v124, v125
	v_and_b32_e32 v124, 1, v124
	v_add_u32_e32 v124, -1, v124
	v_and_b32_e32 v124, 0x38383838, v124
	v_mov_b32_e32 v200, 0
	v_mov_b32_e32 v201, 0
	v_mov_b32_e32 v202, 0
	v_mov_b32_e32 v203, 0
	v_mov_b32_e32 v204, 0
	v_mov_b32_e32 v125, v124
	v_mov_b32_e32 v126, v124
	v_mov_b32_e32 v127, v124
	v_mov_b32_e32 v128, v124
	v_mov_b32_e32 v129, v124
	v_mov_b32_e32 v130, v124
	v_mov_b32_e32 v131, v124
	v_mov_b32_e32 v140, 0x7f7f7f7f
	s_mov_b32 s0, 0xf800000
	s_movk_i32 s15, 0x3000
	s_mov_b32 s12, -1
	s_movk_i32 s14, 0x4000
	s_mov_b32 s13, 0x8000
	v_mov_b32_e32 v132, v141
	v_mov_b32_e32 v133, v141
	v_mov_b32_e32 v134, v141
	v_mov_b32_e32 v135, v141
	v_mov_b32_e32 v136, v141
	v_mov_b32_e32 v137, v141
	v_mov_b32_e32 v138, v141
	v_mov_b32_e32 v139, v141
	s_waitcnt vmcnt(5)
	v_mov_b32_e32 v4, v2
	v_mov_b32_e32 v5, v2
	v_mov_b32_e32 v6, v2
	v_mov_b32_e32 v7, v2
	v_mov_b32_e32 v8, v2
	v_mov_b32_e32 v9, v2
	v_mov_b32_e32 v10, v2
	v_mov_b32_e32 v11, v2
	v_mov_b32_e32 v12, v2
	v_mov_b32_e32 v13, v2
	v_mov_b32_e32 v14, v2
	v_mov_b32_e32 v15, v2
	v_mov_b32_e32 v16, v2
	v_mov_b32_e32 v17, v2
	v_mov_b32_e32 v3, v2
	v_mov_b64_e32 v[18:19], v[16:17]
	v_mov_b64_e32 v[16:17], v[14:15]
	v_mov_b64_e32 v[14:15], v[12:13]
	v_mov_b64_e32 v[12:13], v[10:11]
	v_mov_b64_e32 v[10:11], v[8:9]
	v_mov_b64_e32 v[8:9], v[6:7]
	v_mov_b64_e32 v[6:7], v[4:5]
	v_mov_b64_e32 v[4:5], v[2:3]
	s_waitcnt vmcnt(0) lgkmcnt(0)
	s_barrier
	ds_read_b128 v[24:27], v176 offset:1024
	ds_read_b128 v[20:23], v176
	ds_read_b128 v[36:39], v176 offset:512
	ds_read_b128 v[40:43], v176 offset:1536
	ds_read_b128 v[84:87], v176 offset:16384
	ds_read_b128 v[92:95], v176 offset:16896
	ds_read_b128 v[88:91], v176 offset:17408
	ds_read_b128 v[96:99], v176 offset:17920
	s_waitcnt vmcnt(3) lgkmcnt(6)
	v_mfma_f32_32x32x64_f8f6f4 v[20:35], v[20:27], v[116:123], v[4:19]
	v_mbcnt_lo_u32_b32 v3, -1, 0
	v_mbcnt_hi_u32_b32 v46, -1, v3
	v_and_b32_e32 v3, 64, v46
	v_xor_b32_e32 v47, 32, v46
	v_add_u32_e32 v48, 64, v3
	s_waitcnt vmcnt(2)
	v_max_f32_e32 v3, v44, v44
	s_waitcnt vmcnt(1)
	v_max_f32_e32 v44, v45, v45
	v_max_f32_e32 v44, v44, v3
	v_cmp_lt_i32_e32 vcc, v47, v48
	s_waitcnt vmcnt(0) lgkmcnt(0)
	s_barrier
	s_mov_b32 m0, s33
	s_nop 0
	buffer_load_dwordx4 v174, s[20:23], s15 offen lds
	s_add_i32 s15, s34, 0x4000
	s_mov_b32 m0, s15
	s_nop 0
	buffer_load_dwordx4 v174, s[24:27], s37 offen lds
	s_waitcnt lgkmcnt(4)
	v_mfma_f32_32x32x64_f8f6f4 v[4:19], v[36:43], v[116:123], v[4:19]
	s_nop 1
	v_max_f32_e32 v3, v21, v21
	v_max_f32_e32 v36, v20, v20
	v_max_f32_e32 v3, v36, v3
	v_xor_b32_e32 v38, 16, v46
	s_nop 13
	v_max3_f32 v37, v22, v23, v5
	v_max3_f32 v36, v37, v26, v27
	v_cndmask_b32_e32 v37, v46, v47, vcc
	v_lshlrev_b32_e32 v37, 2, v37
	ds_bpermute_b32 v37, v37, v44
	v_cmp_lt_i32_e32 vcc, v38, v48
	v_max3_f32 v3, v3, v4, v6
	v_max3_f32 v3, v3, v7, v24
	v_cndmask_b32_e32 v38, v46, v38, vcc
	s_waitcnt lgkmcnt(0)
	v_max_f32_e32 v37, v37, v37
	v_max_f32_e32 v37, v44, v37
	v_lshlrev_b32_e32 v38, 2, v38
	ds_bpermute_b32 v38, v38, v37
	v_max3_f32 v36, v36, v10, v11
	v_max3_f32 v3, v3, v25, v8
	v_max3_f32 v36, v36, v30, v31
	v_max3_f32 v3, v3, v9, v28
	s_waitcnt lgkmcnt(0)
	v_max_f32_e32 v38, v38, v38
	v_max_f32_e32 v37, v37, v38
	v_xor_b32_e32 v38, 8, v46
	v_cmp_lt_i32_e32 vcc, v38, v48
	v_max3_f32 v36, v36, v14, v15
	v_max3_f32 v3, v3, v29, v12
	v_cndmask_b32_e32 v38, v46, v38, vcc
	v_lshlrev_b32_e32 v38, 2, v38
	ds_bpermute_b32 v38, v38, v37
	v_max3_f32 v36, v36, v34, v35
	v_max3_f32 v3, v3, v13, v32
	v_max3_f32 v36, v36, v18, v19
	v_max3_f32 v3, v3, v33, v16
	s_waitcnt lgkmcnt(0)
	v_max_f32_e32 v38, v38, v38
	v_max_f32_e32 v37, v37, v38
	v_xor_b32_e32 v38, 4, v46
	v_cmp_lt_i32_e32 vcc, v38, v48
	v_max3_f32 v3, v3, v17, v36
	v_mov_b32_e32 v36, v3
	v_cndmask_b32_e32 v38, v46, v38, vcc
	v_lshlrev_b32_e32 v38, 2, v38
	ds_bpermute_b32 v38, v38, v37
	v_permlane32_swap_b32_e32 v3, v36
	v_max_f32_e32 v36, v36, v36
	v_max_f32_e32 v3, v3, v3
	s_waitcnt lgkmcnt(0)
	v_max_f32_e32 v38, v38, v38
	v_max_f32_e32 v37, v37, v38
	v_xor_b32_e32 v38, 2, v46
	v_cmp_lt_i32_e32 vcc, v38, v48
	v_max_f32_e32 v3, v3, v36
	v_sub_f32_e32 v36, 0xc0400000, v3
	v_cndmask_b32_e32 v38, v46, v38, vcc
	v_lshlrev_b32_e32 v38, 2, v38
	ds_bpermute_b32 v38, v38, v37
	v_add_f32_e32 v20, v36, v20
	v_add_f32_e32 v21, v36, v21
	v_add_f32_e32 v22, v36, v22
	v_add_f32_e32 v23, v36, v23
	s_waitcnt lgkmcnt(0)
	v_max_f32_e32 v38, v38, v38
	v_max_f32_e32 v37, v37, v38
	v_xor_b32_e32 v38, 1, v46
	v_cmp_lt_i32_e32 vcc, v38, v48
	v_add_f32_e32 v24, v36, v24
	v_add_f32_e32 v25, v36, v25
	v_cndmask_b32_e32 v38, v46, v38, vcc
	v_lshlrev_b32_e32 v38, 2, v38
	ds_bpermute_b32 v38, v38, v37
	v_add_f32_e32 v26, v36, v26
	v_add_f32_e32 v27, v36, v27
	v_add_f32_e32 v28, v36, v28
	v_add_f32_e32 v29, v36, v29
	s_waitcnt lgkmcnt(0)
	v_max_f32_e32 v38, v38, v38
	v_max_f32_e32 v37, v37, v38
	v_mul_f32_e32 v38, 0x4f800000, v37
	v_cmp_gt_f32_e32 vcc, s0, v37
	v_add_f32_e32 v30, v36, v30
	v_add_f32_e32 v31, v36, v31
	v_cndmask_b32_e32 v37, v37, v38, vcc
	v_sqrt_f32_e32 v38, v37
	v_add_f32_e32 v32, v36, v32
	v_add_f32_e32 v33, v36, v33
	v_add_f32_e32 v34, v36, v34
	v_add_f32_e32 v35, v36, v35
	v_add_f32_e32 v4, v36, v4
	v_add_f32_e32 v5, v36, v5
	v_add_f32_e32 v6, v36, v6
	v_add_f32_e32 v7, v36, v7
	v_add_f32_e32 v8, v36, v8
	v_add_f32_e32 v9, v36, v9
	v_add_f32_e32 v10, v36, v10
	v_add_f32_e32 v11, v36, v11
	v_add_f32_e32 v12, v36, v12
	v_add_f32_e32 v13, v36, v13
	v_add_f32_e32 v14, v36, v14
	v_add_f32_e32 v15, v36, v15
	v_add_f32_e32 v16, v36, v16
	v_add_f32_e32 v17, v36, v17
	v_add_f32_e32 v18, v36, v18
	v_add_f32_e32 v19, v36, v19
	v_add_u32_e32 v36, -1, v38
	v_fma_f32 v39, -v36, v38, v37
	v_cmp_ge_f32_e64 s[0:1], 0, v39
	v_add_u32_e32 v39, 1, v38
	v_exp_f32_e32 v161, v20
	v_cndmask_b32_e64 v36, v38, v36, s[0:1]
	v_fma_f32 v38, -v39, v38, v37
	v_cmp_lt_f32_e64 s[0:1], 0, v38
	v_exp_f32_e32 v100, v4
	v_exp_f32_e32 v163, v21
	v_cndmask_b32_e64 v36, v36, v39, s[0:1]
	v_mul_f32_e32 v38, 0x37800000, v36
	v_cndmask_b32_e32 v36, v36, v38, vcc
	v_mov_b32_e32 v38, 0x260
	v_cmp_class_f32_e32 vcc, v37, v38
	s_mov_b32 s0, 0x42700000
	v_exp_f32_e32 v148, v5
	v_cndmask_b32_e32 v36, v36, v37, vcc
	s_waitcnt vmcnt(0)
	v_mul_f32_e32 v0, v36, v0
	v_mul_f32_e32 v0, 0x3f91eb85, v0
	v_exp_f32_e32 v162, v22
	v_exp_f32_e32 v101, v6
	v_exp_f32_e32 v164, v23
	v_exp_f32_e32 v102, v7
	v_exp_f32_e32 v150, v24
	v_exp_f32_e32 v143, v8
	v_exp_f32_e32 v154, v25
	v_exp_f32_e32 v146, v9
	v_exp_f32_e32 v152, v26
	v_exp_f32_e32 v145, v10
	v_exp_f32_e32 v157, v27
	v_exp_f32_e32 v147, v11
	v_exp_f32_e32 v149, v28
	v_exp_f32_e32 v69, v12
	v_exp_f32_e32 v153, v29
	v_exp_f32_e32 v109, v13
	v_exp_f32_e32 v151, v30
	v_exp_f32_e32 v108, v14
	v_exp_f32_e32 v156, v31
	v_exp_f32_e32 v142, v15
	v_exp_f32_e32 v155, v32
	v_exp_f32_e32 v110, v16
	v_exp_f32_e32 v159, v33
	v_exp_f32_e32 v144, v17
	v_exp_f32_e32 v158, v34
	v_exp_f32_e32 v111, v18
	v_exp_f32_e32 v160, v35
	v_exp_f32_e32 v114, v19
	v_cmp_nge_f32_e64 s[0:1], s0, v0
	v_sub_f32_e32 v0, v2, v3
	v_add_f32_e32 v36, 0xc0400000, v0
	v_mov_b32_e32 v37, v36
	v_mov_b32_e32 v38, v36
	v_mov_b32_e32 v39, v36
	v_mov_b32_e32 v40, v36
	v_mov_b32_e32 v41, v36
	v_mov_b32_e32 v42, v36
	v_mov_b32_e32 v43, v36
	v_mov_b32_e32 v44, v36
	v_mov_b32_e32 v45, v36
	v_mov_b32_e32 v46, v36
	v_mov_b32_e32 v47, v36
	v_mov_b32_e32 v48, v36
	v_mov_b32_e32 v49, v36
	v_mov_b32_e32 v50, v36
	v_mov_b32_e32 v51, v36
	v_mov_b32_e32 v4, v141
	v_mov_b32_e32 v5, v141
	v_mov_b32_e32 v6, v141
	v_mov_b32_e32 v7, v141
	v_mov_b32_e32 v8, v141
	v_mov_b32_e32 v9, v141
	v_mov_b32_e32 v10, v141
	v_mov_b32_e32 v11, v141
	v_mov_b32_e32 v12, v141
	v_mov_b32_e32 v13, v141
	v_mov_b32_e32 v14, v141
	v_mov_b32_e32 v15, v141
	v_mov_b32_e32 v16, v141
	v_mov_b32_e32 v17, v141
	v_mov_b32_e32 v18, v141
	v_mov_b32_e32 v19, v141
	v_mov_b32_e32 v20, v141
	v_mov_b32_e32 v21, v141
	v_mov_b32_e32 v22, v141
	v_mov_b32_e32 v23, v141
	v_mov_b32_e32 v24, v141
	v_mov_b32_e32 v25, v141
	v_mov_b32_e32 v26, v141
	v_mov_b32_e32 v27, v141
	v_mov_b32_e32 v28, v141
	v_mov_b32_e32 v29, v141
	v_mov_b32_e32 v30, v141
	v_mov_b32_e32 v31, v141
	v_mov_b32_e32 v32, v141
	v_mov_b32_e32 v33, v141
	v_mov_b32_e32 v34, v141
	v_mov_b32_e32 v35, v141
	v_mov_b32_e32 v0, v141

.LBB1_5:
	s_waitcnt lgkmcnt(6)
	v_mfma_f32_32x32x64_f8f6f4 v[4:19], v[156:163], v[148:155], v[4:19]
	v_cmp_eq_u32_e32 vcc, 0, v1
	s_nop 1
	s_and_saveexec_b64 s[0:1], vcc
	s_lshl_b32 s12, s29, 2
	s_add_i32 s12, s12, 0x12000
	v_mov_b32_e32 v1, s12
	ds_write_b32 v1, v0
	s_or_b64 exec, exec, s[0:1]
	s_waitcnt vmcnt(0) lgkmcnt(0)
	s_barrier
	s_waitcnt lgkmcnt(4)
	v_mfma_f32_32x32x64_f8f6f4 v[20:35], v[164:171], v[148:155], v[20:35]
	s_waitcnt lgkmcnt(1)
	v_mfma_f32_32x32x64_f8f6f4 v[4:19], v[80:87], v[72:79], v[4:19]
	v_mov_b32_e32 v104, 0x12000
	ds_read_b128 v[38:41], v104
	ds_read_b128 v[42:45], v104 offset:16
	s_mov_b32 s14, 0
	s_waitcnt lgkmcnt(0)
	v_or_b32_e32 v0, v39, v38
	v_or_b32_e32 v0, v40, v0
	v_or_b32_e32 v0, v41, v0
	v_or_b32_e32 v0, v42, v0
	v_or_b32_e32 v0, v43, v0
	v_or_b32_e32 v0, v44, v0
	v_or_b32_e32 v0, v45, v0
	v_mfma_f32_32x32x64_f8f6f4 v[20:35], v[58:65], v[72:79], v[20:35]
	v_cmp_ne_u32_e32 vcc, 0, v0
	s_cbranch_vccnz .LBB1_13
	s_mov_b64 s[0:1], -1
	s_nop 2
	v_mov_b32_e32 v54, v4
	s_nop 15
	v_mov_b32_e32 v38, v20
	v_mov_b32_e32 v55, v5
	v_mov_b32_e32 v39, v21
	v_mov_b32_e32 v56, v6
	v_mov_b32_e32 v40, v22
	v_mov_b32_e32 v57, v7
	v_mov_b32_e32 v41, v23
	v_mov_b32_e32 v58, v8
	v_mov_b32_e32 v42, v24
	v_mov_b32_e32 v59, v9
	v_mov_b32_e32 v43, v25
	v_mov_b32_e32 v60, v10
	v_mov_b32_e32 v44, v26
	v_mov_b32_e32 v61, v11
	v_mov_b32_e32 v45, v27
	v_mov_b32_e32 v62, v12
	v_mov_b32_e32 v46, v28
	v_mov_b32_e32 v63, v13
	v_mov_b32_e32 v47, v29
	v_mov_b32_e32 v64, v14
	v_mov_b32_e32 v48, v30
	v_mov_b32_e32 v65, v15
	v_mov_b32_e32 v49, v31
	v_mov_b32_e32 v66, v16
	v_mov_b32_e32 v50, v32
	v_mov_b32_e32 v67, v17
	v_mov_b32_e32 v51, v33
	v_mov_b32_e32 v68, v18
	v_mov_b32_e32 v52, v34
	v_mov_b32_e32 v69, v19
	v_mov_b32_e32 v53, v35
	s_branch .Lfinal_copy

.Lfinal_copy:
	v_mov_b64_e32 v[100:101], v[18:19]
	v_mov_b64_e32 v[84:85], v[34:35]
	v_mul_f32_e32 v141, 0.5, v200
	v_mov_b64_e32 v[98:99], v[16:17]
	v_mov_b64_e32 v[96:97], v[14:15]
	v_mov_b64_e32 v[94:95], v[12:13]
	v_mov_b64_e32 v[92:93], v[10:11]
	v_mov_b64_e32 v[90:91], v[8:9]
	v_mov_b64_e32 v[88:89], v[6:7]
	v_mov_b64_e32 v[86:87], v[4:5]
	v_mov_b64_e32 v[82:83], v[32:33]
	v_mov_b64_e32 v[80:81], v[30:31]
	v_mov_b64_e32 v[78:79], v[28:29]
	v_mov_b64_e32 v[76:77], v[26:27]
	v_mov_b64_e32 v[74:75], v[24:25]
	v_mov_b64_e32 v[72:73], v[22:23]
	v_mov_b64_e32 v[70:71], v[20:21]
	v_mov_b32_e32 v146, v3
